# v5 + P3: waves 4..7 run the conv items before the per-row work (block order swapped per wave half)
# baseline (speedup 1.0000x reference)
.LBB0_729:
	s_cmp_lt_i32 s92, 4
	s_cselect_b64 s[0:1], -1, 0
	s_cmp_gt_i32 s93, 3
	s_cselect_b64 s[2:3], -1, 0
	s_and_b64 s[0:1], s[0:1], s[2:3]
	s_andn2_b64 vcc, exec, s[0:1]
	s_cbranch_vccnz .LBB0_996
	s_mov_b32 s98, 0
.Lp3_pro:
	v_mov_b32_e32 v1, v0
	s_lshl_b32 s6, s90, 3
	v_readfirstlane_b32 s0, v1
	s_ashr_i32 s2, s0, 6
	v_and_b32_e32 v34, 63, v1
	s_add_i32 s3, s2, s6
	s_lshl_b32 s10, s84, 3
	v_lshlrev_b32_e32 v1, 3, v34
	s_cmpk_gt_i32 s3, 0x1fff
	v_mov_b32_e32 v41, 0
	s_cbranch_scc1 .LBB0_743
	s_bitcmp1_b32 s2, 2
	s_cbranch_scc0 .Lp3_rows
	s_cmp_lg_u32 s98, 0
	s_cbranch_scc1 .Lp3_rows
	s_mov_b32 s98, 2
	s_branch .LBB0_743
.Lp3_rows:
	v_readlane_b32 s12, v254, 19
	v_readlane_b32 s13, v254, 20
	v_readlane_b32 s14, v254, 21
	v_readlane_b32 s15, v254, 22
	v_readlane_b32 s24, v254, 31
	v_readlane_b32 s25, v254, 32
	v_readlane_b32 s26, v254, 33
	v_readlane_b32 s27, v254, 34
	s_mov_b64 s[12:13], s[24:25]
	s_waitcnt vmcnt(15)
	v_lshlrev_b32_e32 v26, 2, v1
	v_lshlrev_b32_e32 v40, 2, v34
	s_mov_b64 s[14:15], s[26:27]
	global_load_dword v43, v40, s[60:61]
	global_load_dword v48, v40, s[62:63]
	global_load_dwordx4 v[2:5], v26, s[14:15] offset:16
	global_load_dwordx4 v[6:9], v26, s[12:13] offset:16
	global_load_dwordx4 v[10:13], v26, s[14:15]
	global_load_dwordx4 v[14:17], v26, s[12:13]
	global_load_dwordx4 v[18:21], v26, s[12:13] offset:2064
	global_load_dwordx4 v[22:25], v26, s[12:13] offset:2048
	s_ashr_i32 s7, s2, 31
	s_ashr_i32 s8, s6, 31
	s_add_u32 s6, s2, s6
	s_addc_u32 s7, s7, s8
	s_lshl_b64 s[8:9], s[6:7], 5
	v_lshl_add_u64 v[26:27], s[8:9], 0, v[40:41]
	s_lshl_b64 s[8:9], s[6:7], 7
	v_readlane_b32 s20, v254, 27
	v_readlane_b32 s21, v254, 28
	v_lshl_or_b32 v28, v34, 1, s8
	v_mov_b32_e32 v29, s9
	s_waitcnt vmcnt(22)
	v_lshl_add_u64 v[30:31], s[8:9], 0, v[40:41]
	s_mov_b64 s[8:9], 0xa700000
	v_lshl_add_u64 v[30:31], v[30:31], 0, s[8:9]
	s_lshl_b64 s[8:9], s[6:7], 10
	s_lshl_b64 s[20:21], s[6:7], 11
	v_lshlrev_b32_e32 v38, 4, v34
	v_mov_b32_e32 v39, v41
	v_mov_b32_e32 v41, 0xee00
	v_readlane_b32 s22, v254, 29
	v_readlane_b32 s23, v254, 30
	v_cmp_gt_u32_e32 vcc, 32, v34
	v_cmp_gt_u32_e64 s[0:1], 16, v34
	v_cmp_lt_u32_e64 s[4:5], 7, v34
	v_mov_b32_e32 v33, s9
	v_or_b32_e32 v34, s20, v38
	s_waitcnt vmcnt(21)
	v_or_b32_e32 v44, s8, v38
	v_mov_b32_e32 v45, s9
	s_mul_i32 s9, s7, 0xee00
	v_mad_u64_u32 v[38:39], s[6:7], s6, v41, v[38:39]
	s_mov_b64 s[22:23], 0x9e00000
	v_add_u32_e32 v39, s9, v39
	s_mov_b64 s[6:7], 0x29f00400
	v_lshl_add_u64 v[36:37], v[44:45], 0, s[22:23]
	v_lshl_add_u64 v[38:39], v[38:39], 0, s[6:7]
	v_or_b32_e32 v44, s8, v40
	s_mov_b64 s[6:7], 0xa900100
	s_ashr_i32 s11, s10, 31
	s_mov_b64 s[14:15], 0xa600000
	v_lshl_add_u64 v[40:41], v[44:45], 0, s[6:7]
	s_mov_b32 s38, 0x3c800000
	s_lshl_b64 s[12:13], s[10:11], 5
	v_lshl_add_u64 v[28:29], v[28:29], 0, s[14:15]
	s_lshl_b64 s[14:15], s[10:11], 7
	v_or_b32_e32 v32, s8, v1
	s_lshl_b64 s[52:53], s[10:11], 10
	v_mov_b32_e32 v35, s21
	s_lshl_b64 s[54:55], s[10:11], 11
	s_mul_hi_i32 s57, s10, 0xee00
	s_mul_i32 s56, s10, 0xee00
	v_mov_b32_e32 v42, 0x358637bd
	s_mov_b32 s11, 0x800000
	s_mov_b32 s33, 0x8e00000
	s_mov_b32 s34, 0xc3e00000
	s_mov_b32 s35, 0x15100000
	s_mov_b32 s39, 0x3b000000
	s_mov_b32 s36, 0x3f200000
	s_mov_b32 s37, 0x3fb8aa3b
	s_mov_b32 s42, 0xc2ce8ed0
	s_mov_b32 s43, 0x42b17218
	s_mov_b32 s44, 0x7f800000
	v_mov_b32_e32 v49, 0x3ca908c9
	s_brev_b32 s45, -2
	s_mov_b32 s46, 0xbfb8aa3b
	s_mov_b32 s47, 0x3f2aaaab
	s_waitcnt vmcnt(20)
	v_mov_b32_e32 v50, 0x3ecc95a3
	s_mov_b32 s48, 0x3f317218
	s_mov_b32 s49, 0x33800000
	v_mov_b32_e32 v51, 0x43e00000
	v_mov_b32_e32 v52, 0x7f800000
	v_mov_b32_e32 v44, 0x3f317218
	v_mov_b32_e32 v53, 0x7fc00000
	v_mov_b32_e32 v54, 0xff800000
	s_mov_b32 s50, s3
	v_readlane_b32 s16, v254, 23
	v_readlane_b32 s17, v254, 24
	v_readlane_b32 s18, v254, 25
	v_readlane_b32 s19, v254, 26
	s_branch .LBB0_734

.LBB0_743:
	s_cmp_eq_u32 s98, 3
	s_cbranch_scc1 .LBB0_946
	s_cmpk_gt_i32 s3, 0x7ff
	s_cbranch_scc1 .LBB0_946
	v_readlane_b32 s12, v254, 3
	v_readlane_b32 s13, v254, 4
	v_readlane_b32 s14, v254, 5
	v_readlane_b32 s15, v254, 6
	v_readlane_b32 s16, v254, 7
	v_readlane_b32 s17, v254, 8
	v_readlane_b32 s18, v254, 9
	v_readlane_b32 s19, v254, 10
	v_readlane_b32 s20, v254, 11
	v_readlane_b32 s21, v254, 12
	v_readlane_b32 s22, v254, 13
	v_readlane_b32 s23, v254, 14
	v_readlane_b32 s24, v254, 15
	v_readlane_b32 s25, v254, 16
	v_readlane_b32 s26, v254, 17
	v_readlane_b32 s27, v254, 18
	s_mov_b64 s[12:13], s[20:21]
	s_mov_b64 s[18:19], s[26:27]
	s_mov_b64 s[14:15], s[22:23]
	s_add_u32 s11, s18, 0x29f00000
	s_addc_u32 s15, s19, 0
	s_add_u32 s4, s18, 0xb100000
	s_addc_u32 s5, s19, 0
	s_lshl_b32 s0, s90, 12
	s_lshl_b32 s1, s2, 9
	s_mov_b64 s[16:17], s[24:25]
	s_add_i32 s22, s0, s1
	s_lshl_b32 s0, s90, 5
	s_lshl_b32 s1, s2, 2
	s_lshl_b32 s23, s84, 12
	s_add_i32 s35, s0, s1
	s_lshl_b32 s38, s84, 5
	v_mov_b32_e32 v183, 0
	s_mov_b64 s[6:7], 0x4000
	s_mov_b64 s[8:9], 0x8000
	s_mov_b64 s[12:13], 0xc000
	s_mov_b32 s14, 0x3d800000
	s_branch .LBB0_746

.LBB0_946:
	s_cmp_eq_u32 s98, 2
	s_cbranch_scc0 .Lp3_end
	s_mov_b32 s98, 3
	s_branch .Lp3_pro
